# proj GEMM: each wave owns 64 contiguous output columns (B half-step 32 rows, re-spaced B-row permutation); epilogue pairs the bj=0/bj=1 row pieces via permlane32/16 swaps into 16-byte-per-lane stores
# baseline (speedup 1.0000x reference)
.LBB0_225:
	s_andn2_b64 vcc, exec, s[0:1]
	v_writelane_b32 v252, s46, 58
	s_cbranch_vccnz .LBB0_390
	v_readlane_b32 s4, v251, 4
	v_readlane_b32 s0, v251, 49
	v_readlane_b32 s5, v251, 5
	v_mov_b32_e32 v1, v0
	s_waitcnt vmcnt(0)
	v_mov_b32_e32 v12, v0
	v_readlane_b32 s1, v251, 50
	s_andn2_b64 vcc, exec, s[0:1]
	v_readfirstlane_b32 s17, v12
	s_cbranch_vccnz .LBB0_344
	v_lshlrev_b32_e32 v1, 4, v12
	v_add_u32_e32 v3, 0x2000, v1
	v_ashrrev_i32_e32 v4, 31, v3
	v_lshrrev_b32_e32 v4, 22, v4
	v_add_u32_e32 v4, v3, v4
	v_ashrrev_i32_e32 v13, 10, v4
	v_mul_i32_i24_e32 v4, 0x400, v13
	s_load_dwordx2 s[12:13], s[4:5], 0xc8
	s_load_dwordx4 s[0:3], s[4:5], 0x40
	v_sub_u32_e32 v3, v3, v4
	v_lshrrev_b32_e32 v4, 4, v3
	v_bitop3_b32 v3, v4, v3, 32 bitop3:0x6c
	v_ashrrev_i32_e32 v4, 31, v3
	s_waitcnt lgkmcnt(0)
	s_add_u32 s30, s12, 0xd400000
	v_lshrrev_b32_e32 v4, 26, v4
	s_mul_i32 s4, s46, 0x500000
	s_addc_u32 s31, s13, 0
	v_add_u32_e32 v4, v3, v4
	v_lshlrev_b32_e32 v5, 3, v13
	s_add_u32 s4, s12, s4
	v_ashrrev_i32_e32 v14, 6, v4
	v_and_b32_e32 v5, -16, v5
	s_addc_u32 s5, s13, 0
	v_add_u32_e32 v5, v14, v5
	s_add_u32 s34, s4, 0x1c00000
	v_and_b32_e32 v6, 3, v14
	s_mov_b32 s4, 0x3fffe0
	v_lshrrev_b32_e32 v7, 2, v5
	v_lshlrev_b32_e32 v8, 1, v5
	v_and_b32_e32 v4, 0xc0, v4
	v_and_or_b32 v6, v5, s4, v6
	v_and_b32_e32 v7, 4, v7
	v_and_b32_e32 v8, 24, v8
	v_sub_u32_e32 v3, v3, v4
	v_or3_b32 v6, v6, v7, v8
	v_lshlrev_b32_e32 v7, 5, v13
	v_ashrrev_i16_sdwa v3, v211, sext(v3) dst_sel:DWORD dst_unused:UNUSED_PAD src0_sel:DWORD src1_sel:BYTE_0
	v_and_b32_e32 v7, 32, v7
	v_bfe_i32 v15, v3, 0, 16
	v_add_lshl_u32 v3, v7, v15, 1
	v_lshl_add_u32 v172, v6, 10, v3
	v_lshl_add_u32 v174, v5, 10, v3
	v_bfe_i32 v3, v12, 27, 1
	v_lshrrev_b32_e32 v3, 22, v3
	v_add_u32_e32 v3, v1, v3
	v_and_b32_e32 v3, 0xfffffc00, v3
	v_sub_u32_e32 v1, v1, v3
	v_lshrrev_b32_e32 v3, 4, v1
	v_ashrrev_i32_e32 v4, 31, v12
	v_bitop3_b32 v1, v3, v1, 32 bitop3:0x6c
	v_lshrrev_b32_e32 v4, 26, v4
	v_ashrrev_i32_e32 v3, 31, v1
	v_add_u32_e32 v4, v12, v4
	v_lshrrev_b32_e32 v3, 26, v3
	v_ashrrev_i32_e32 v17, 6, v4
	v_add_u32_e32 v3, v1, v3
	v_lshlrev_b32_e32 v4, 3, v17
	v_ashrrev_i32_e32 v16, 6, v3
	v_and_b32_e32 v4, -16, v4
	s_addc_u32 s35, s5, 0
	s_ashr_i32 s18, s17, 6
	v_add_u32_e32 v4, v16, v4
	v_and_b32_e32 v5, 3, v16
	s_ashr_i32 s16, s17, 8
	s_lshl_b32 s36, s18, 10
	v_and_or_b32 v5, v4, s4, v5
	v_lshrrev_b32_e32 v6, 2, v4
	v_lshlrev_b32_e32 v7, 1, v4
	v_and_b32_e32 v3, 0xc0, v3
	v_readlane_b32 s4, v252, 46
	v_and_b32_e32 v6, 4, v6
	v_and_b32_e32 v7, 24, v7
	v_sub_u32_e32 v1, v1, v3
	v_readlane_b32 s5, v252, 47
	s_add_u32 s6, s30, s4
	v_or3_b32 v5, v5, v6, v7
	v_lshlrev_b32_e32 v6, 5, v17
	v_ashrrev_i16_sdwa v1, v211, sext(v1) dst_sel:DWORD dst_unused:UNUSED_PAD src0_sel:DWORD src1_sel:BYTE_0
	s_addc_u32 s7, s31, s5
	v_readlane_b32 s4, v252, 50
	v_and_b32_e32 v6, 32, v6
	v_bfe_i32 v18, v1, 0, 16
	v_readlane_b32 s5, v252, 51
	s_add_u32 s4, s34, s4
	v_add_lshl_u32 v1, v6, v18, 1
	s_addc_u32 s5, s35, s5
	s_add_i32 s37, s36, 0
	v_lshl_add_u32 v176, v5, 10, v1
	v_and_b32_e32 v244, 0x18000, v176
	v_add_u32_e32 v176, v176, v244
	v_and_b32_e32 v244, 0x18000, v172
	v_add_u32_e32 v172, v172, v244
	v_lshl_add_u32 v178, v4, 10, v1
	v_mov_b32_e32 v1, 0x7f7f7f7f
	s_add_i32 m0, s37, 0x10000
	v_mov_b32_e32 v177, v2
	global_load_lds_dwordx4 v176, s[4:5]
	s_add_i32 m0, s37, 0x12000
	s_add_u32 s8, s4, 0x8000
	global_load_lds_dwordx4 v172, s[4:5]
	s_addc_u32 s9, s5, 0
	s_add_i32 m0, s37, 0x14000
	s_add_i32 s38, s37, 0x2000
	global_load_lds_dwordx4 v176, s[8:9]
	s_add_i32 m0, s37, 0x16000
	v_mov_b32_e32 v173, v2
	global_load_lds_dwordx4 v172, s[8:9]
	s_mov_b32 m0, s37
	s_add_u32 s8, s6, 0x20000
	global_load_lds_dwordx4 v178, s[6:7]
	s_mov_b32 m0, s38
	s_addc_u32 s9, s7, 0
	s_add_i32 s39, s37, 0x4000
	global_load_lds_dwordx4 v174, s[6:7]
	s_mov_b32 m0, s39
	s_add_i32 s42, s37, 0x6000
	global_load_lds_dwordx4 v178, s[8:9]
	s_mov_b32 m0, s42
	v_mov_b32_e32 v179, v2
	global_load_lds_dwordx4 v174, s[8:9]
	v_mov_b32_e32 v175, v2
	s_cmp_eq_u32 s16, 1
	v_lshl_add_u64 v[10:11], s[4:5], 0, v[176:177]
	v_lshl_add_u64 v[8:9], s[4:5], 0, v[172:173]
	v_lshl_add_u64 v[4:5], s[6:7], 0, v[178:179]
	s_cselect_b64 s[8:9], -1, 0
	s_cmp_lg_u32 s16, 1
	v_lshl_add_u64 v[6:7], s[6:7], 0, v[174:175]
	s_cbranch_scc1 .LBB0_229
	s_barrier
.LBB0_229:
	s_lshl_b32 s52, s46, 2
	s_add_u32 s10, s12, 0x11400000
	s_addc_u32 s11, s13, 0
	s_add_u32 s12, s12, 0x400000
	s_addc_u32 s13, s13, 0
	s_lshl_b64 s[20:21], s[52:53], 2
	s_add_u32 s14, s0, s20
	s_addc_u32 s15, s1, s21
	s_add_u32 s2, s2, s20
	s_mov_b64 s[0:1], 0x80
	s_addc_u32 s3, s3, s21
	v_lshl_add_u64 v[10:11], v[10:11], 0, s[0:1]
	s_add_i32 m0, s37, 0x18000
	s_and_b32 s43, s18, 3
	s_waitcnt vmcnt(2)
	s_barrier
	global_load_lds_dwordx4 v[10:11], off
	v_lshl_add_u64 v[8:9], v[8:9], 0, s[0:1]
	s_add_i32 m0, s37, 0x1a000
	s_add_i32 s45, s37, 0x8000
	s_lshl_b32 s44, s16, 6
	s_lshl_b32 s18, s16, 13
	s_lshl_b32 s16, s43, 6
	s_lshl_b32 s19, s43, 12
	global_load_lds_dwordx4 v[8:9], off
	v_lshl_add_u64 v[4:5], v[4:5], 0, s[0:1]
	s_mov_b32 m0, s45
	s_add_i32 s46, s37, 0xa000
	global_load_lds_dwordx4 v[4:5], off
	v_lshl_add_u64 v[4:5], v[6:7], 0, s[0:1]
	s_add_u32 s0, s4, 0x8080
	s_mov_b32 m0, s46
	s_addc_u32 s1, s5, 0
	global_load_lds_dwordx4 v[4:5], off
	v_lshl_add_u64 v[4:5], s[0:1], 0, v[176:177]
	s_add_i32 m0, s37, 0x1c000
	v_and_b32_e32 v3, 15, v12
	global_load_lds_dwordx4 v[4:5], off
	v_lshl_add_u64 v[4:5], s[0:1], 0, v[172:173]
	s_add_i32 m0, s37, 0x1e000
	v_lshlrev_b32_e32 v7, 2, v12
	global_load_lds_dwordx4 v[4:5], off
	v_lshlrev_b32_e32 v4, 1, v12
	v_and_b32_e32 v4, 32, v4
	v_lshlrev_b32_e32 v5, 5, v12
	v_lshlrev_b32_e32 v6, 6, v3
	v_and_b32_e32 v7, 32, v7
	v_and_b32_e32 v5, 0x400, v5
	v_bitop3_b32 v4, v6, v7, v4 bitop3:0x36
	v_or3_b32 v6, v4, s18, v5
	v_or3_b32 v192, v4, s19, v5
	v_and_b32_e32 v249, 16, v0
	v_xor_b32_e32 v192, v192, v249
	v_add_u32_e32 v192, 0x10000, v192
	v_xor_b32_e32 v249, 16, v192
	v_lshlrev_b32_e32 v4, 13, v17
	v_and_b32_e32 v4, 0xffffc000, v4
	v_lshl_add_u32 v4, v16, 10, v4
	v_and_b32_e32 v5, 1, v17
	v_lshl_or_b32 v4, v5, 6, v4
	v_lshl_add_u32 v180, v18, 1, v4
	v_lshlrev_b32_e32 v4, 13, v13
	v_and_b32_e32 v4, 0xffffc000, v4
	v_readlane_b32 s0, v252, 48
	s_waitcnt vmcnt(6)
	v_lshl_add_u32 v4, v14, 10, v4
	v_and_b32_e32 v5, 1, v13
	v_readlane_b32 s1, v252, 49
	s_cmpk_lt_u32 s17, 0x100
	v_lshl_or_b32 v4, v5, 6, v4
	s_mov_b32 s33, s0
	v_readlane_b32 s0, v252, 44
	v_bfe_u32 v170, v12, 4, 2
	s_cselect_b64 s[18:19], -1, 0
	s_mov_b32 s17, s53
	v_mov_b32_e32 v181, v2
	v_lshl_add_u32 v182, v15, 1, v4
	v_mov_b32_e32 v183, v2
	s_mov_b32 s47, 0
	v_add_u32_e32 v193, 0, v6
	v_and_b32_e32 v250, 16, v0
	v_xor_b32_e32 v193, v193, v250
	v_xor_b32_e32 v250, 16, v193
	s_mov_b32 s28, s0
	s_barrier
	v_readlane_b32 s1, v252, 45
	s_branch .LBB0_232

.LBB0_235:
	s_add_u32 s4, s0, 0xfffe0080
	s_addc_u32 s5, s1, -1
	s_add_i32 s52, 0, 0x10000
	s_cmp_eq_u32 s51, 4
	s_cselect_b32 s7, s21, s5
	s_cselect_b32 s6, s29, s4
	s_cselect_b32 s5, s23, s50
	s_cselect_b32 s4, s48, s49
	s_add_i32 s53, 0, 0x14000
	ds_read_b128 v[20:23], v192
	ds_read_b128 v[24:27], v249
	ds_read_b128 v[28:31], v192 offset:2048
	ds_read_b128 v[32:35], v249 offset:2048
	ds_read_b128 v[4:7], v192 offset:16384
	ds_read_b128 v[8:11], v249 offset:16384
	ds_read_b128 v[12:15], v192 offset:18432
	ds_read_b128 v[16:19], v249 offset:18432
	v_lshl_add_u64 v[234:235], s[0:1], 0, v[180:181]
	s_add_i32 m0, s37, 0xc000
	ds_read_b128 v[184:187], v193
	ds_read_b128 v[188:191], v250
	ds_read_b128 v[194:197], v193 offset:2048
	ds_read_b128 v[198:201], v250 offset:2048
	ds_read_b128 v[202:205], v193 offset:4096
	ds_read_b128 v[206:209], v250 offset:4096
	ds_read_b128 v[226:229], v193 offset:6144
	ds_read_b128 v[230:233], v250 offset:6144
	global_load_lds_dwordx4 v[234:235], off
	v_lshl_add_u64 v[234:235], s[0:1], 0, v[182:183]
	s_add_i32 m0, s37, 0xe000
	s_nop 0
	global_load_lds_dwordx4 v[234:235], off
	s_waitcnt vmcnt(8)
	s_waitcnt lgkmcnt(0)
	s_barrier
	s_setprio 1
	s_waitcnt lgkmcnt(0)
	v_mfma_scale_f32_16x16x128_f8f6f4 v[96:99], v[20:27], v[184:191], v[96:99], v1, v1 op_sel_hi:[0,0,0]
	v_mfma_scale_f32_16x16x128_f8f6f4 v[92:95], v[28:35], v[184:191], v[92:95], v1, v1 op_sel_hi:[0,0,0]
	v_mfma_scale_f32_16x16x128_f8f6f4 v[88:91], v[20:27], v[194:201], v[88:91], v1, v1 op_sel_hi:[0,0,0]
	v_mfma_scale_f32_16x16x128_f8f6f4 v[84:87], v[28:35], v[194:201], v[84:87], v1, v1 op_sel_hi:[0,0,0]
	v_mfma_scale_f32_16x16x128_f8f6f4 v[80:83], v[20:27], v[202:209], v[80:83], v1, v1 op_sel_hi:[0,0,0]
	v_mfma_scale_f32_16x16x128_f8f6f4 v[76:79], v[28:35], v[202:209], v[76:79], v1, v1 op_sel_hi:[0,0,0]
	v_mfma_scale_f32_16x16x128_f8f6f4 v[72:75], v[20:27], v[226:233], v[72:75], v1, v1 op_sel_hi:[0,0,0]
	v_mfma_scale_f32_16x16x128_f8f6f4 v[68:71], v[28:35], v[226:233], v[68:71], v1, v1 op_sel_hi:[0,0,0]
	s_setprio 0
	s_setprio 1
	v_mfma_scale_f32_16x16x128_f8f6f4 v[160:163], v[4:11], v[184:191], v[160:163], v1, v1 op_sel_hi:[0,0,0]
	v_mfma_scale_f32_16x16x128_f8f6f4 v[156:159], v[12:19], v[184:191], v[156:159], v1, v1 op_sel_hi:[0,0,0]
	v_mfma_scale_f32_16x16x128_f8f6f4 v[152:155], v[4:11], v[194:201], v[152:155], v1, v1 op_sel_hi:[0,0,0]
	v_mfma_scale_f32_16x16x128_f8f6f4 v[148:151], v[12:19], v[194:201], v[148:151], v1, v1 op_sel_hi:[0,0,0]
	v_mfma_scale_f32_16x16x128_f8f6f4 v[144:147], v[4:11], v[202:209], v[144:147], v1, v1 op_sel_hi:[0,0,0]
	v_mfma_scale_f32_16x16x128_f8f6f4 v[140:143], v[12:19], v[202:209], v[140:143], v1, v1 op_sel_hi:[0,0,0]
	v_mfma_scale_f32_16x16x128_f8f6f4 v[136:139], v[4:11], v[226:233], v[136:139], v1, v1 op_sel_hi:[0,0,0]
	v_mfma_scale_f32_16x16x128_f8f6f4 v[132:135], v[12:19], v[226:233], v[132:135], v1, v1 op_sel_hi:[0,0,0]
	s_setprio 0
	s_barrier
	s_add_i32 s52, s52, s36
	v_lshl_add_u64 v[184:185], s[4:5], 0, v[176:177]
	s_mov_b32 m0, s52
	ds_read_b128 v[194:197], v193 offset:16384
	ds_read_b128 v[198:201], v250 offset:16384
	ds_read_b128 v[202:205], v193 offset:18432
	ds_read_b128 v[206:209], v250 offset:18432
	ds_read_b128 v[226:229], v193 offset:20480
	ds_read_b128 v[230:233], v250 offset:20480
	ds_read_b128 v[234:237], v193 offset:22528
	ds_read_b128 v[238:241], v250 offset:22528
	global_load_lds_dwordx4 v[184:185], off
	s_add_i32 m0, s52, 0x2000
	s_add_u32 s54, s4, 0x8000
	v_lshl_add_u64 v[186:187], s[4:5], 0, v[172:173]
	s_addc_u32 s55, s5, 0
	s_add_i32 s52, s53, s36
	global_load_lds_dwordx4 v[186:187], off
	v_lshl_add_u64 v[188:189], s[54:55], 0, v[176:177]
	s_mov_b32 m0, s52
	v_lshl_add_u64 v[190:191], s[6:7], 0, v[174:175]
	global_load_lds_dwordx4 v[188:189], off
	v_lshl_add_u64 v[188:189], s[54:55], 0, v[172:173]
	s_add_i32 m0, s52, 0x2000
	s_nop 0
	global_load_lds_dwordx4 v[188:189], off
	v_lshl_add_u64 v[188:189], s[6:7], 0, v[178:179]
	s_mov_b32 m0, s37
	s_nop 0
	global_load_lds_dwordx4 v[188:189], off
	s_mov_b32 m0, s38
	s_nop 0
	global_load_lds_dwordx4 v[190:191], off
	s_waitcnt vmcnt(8)
	s_waitcnt lgkmcnt(0)
	s_barrier
	s_setprio 1
	s_waitcnt lgkmcnt(0)
	v_mfma_scale_f32_16x16x128_f8f6f4 v[64:67], v[20:27], v[194:201], v[64:67], v1, v1 op_sel_hi:[0,0,0]
	v_mfma_scale_f32_16x16x128_f8f6f4 v[60:63], v[28:35], v[194:201], v[60:63], v1, v1 op_sel_hi:[0,0,0]
	v_mfma_scale_f32_16x16x128_f8f6f4 v[56:59], v[20:27], v[202:209], v[56:59], v1, v1 op_sel_hi:[0,0,0]
	v_mfma_scale_f32_16x16x128_f8f6f4 v[52:55], v[28:35], v[202:209], v[52:55], v1, v1 op_sel_hi:[0,0,0]
	v_mfma_scale_f32_16x16x128_f8f6f4 v[48:51], v[20:27], v[226:233], v[48:51], v1, v1 op_sel_hi:[0,0,0]
	v_mfma_scale_f32_16x16x128_f8f6f4 v[44:47], v[28:35], v[226:233], v[44:47], v1, v1 op_sel_hi:[0,0,0]
	v_mfma_scale_f32_16x16x128_f8f6f4 v[40:43], v[20:27], v[234:241], v[40:43], v1, v1 op_sel_hi:[0,0,0]
	v_mfma_scale_f32_16x16x128_f8f6f4 v[36:39], v[28:35], v[234:241], v[36:39], v1, v1 op_sel_hi:[0,0,0]
	s_setprio 0
	s_setprio 1
	v_mfma_scale_f32_16x16x128_f8f6f4 v[128:131], v[4:11], v[194:201], v[128:131], v1, v1 op_sel_hi:[0,0,0]
	v_mfma_scale_f32_16x16x128_f8f6f4 v[124:127], v[12:19], v[194:201], v[124:127], v1, v1 op_sel_hi:[0,0,0]
	v_mfma_scale_f32_16x16x128_f8f6f4 v[120:123], v[4:11], v[202:209], v[120:123], v1, v1 op_sel_hi:[0,0,0]
	v_mfma_scale_f32_16x16x128_f8f6f4 v[116:119], v[12:19], v[202:209], v[116:119], v1, v1 op_sel_hi:[0,0,0]
	v_mfma_scale_f32_16x16x128_f8f6f4 v[112:115], v[4:11], v[226:233], v[112:115], v1, v1 op_sel_hi:[0,0,0]
	v_mfma_scale_f32_16x16x128_f8f6f4 v[108:111], v[12:19], v[226:233], v[108:111], v1, v1 op_sel_hi:[0,0,0]
	v_mfma_scale_f32_16x16x128_f8f6f4 v[104:107], v[4:11], v[234:241], v[104:107], v1, v1 op_sel_hi:[0,0,0]
	v_mfma_scale_f32_16x16x128_f8f6f4 v[100:103], v[12:19], v[234:241], v[100:103], v1, v1 op_sel_hi:[0,0,0]
	s_setprio 0
	s_barrier
	s_add_i32 s52, 0, 0x18000
	s_add_i32 s53, 0, 0x1c000
	ds_read_b128 v[4:7], v192 offset:32768
	ds_read_b128 v[8:11], v249 offset:32768
	ds_read_b128 v[12:15], v192 offset:34816
	ds_read_b128 v[16:19], v249 offset:34816
	ds_read_b128 v[20:23], v192 offset:49152
	ds_read_b128 v[24:27], v249 offset:49152
	ds_read_b128 v[28:31], v192 offset:51200
	ds_read_b128 v[32:35], v249 offset:51200
	s_add_u32 s6, s6, 0x20000
	s_addc_u32 s7, s7, 0
	s_mov_b32 m0, s39
	v_lshl_add_u64 v[242:243], s[6:7], 0, v[178:179]
	ds_read_b128 v[194:197], v193 offset:32768
	ds_read_b128 v[198:201], v250 offset:32768
	ds_read_b128 v[202:205], v193 offset:34816
	ds_read_b128 v[206:209], v250 offset:34816
	ds_read_b128 v[226:229], v193 offset:36864
	ds_read_b128 v[230:233], v250 offset:36864
	ds_read_b128 v[234:237], v193 offset:38912
	ds_read_b128 v[238:241], v250 offset:38912
	global_load_lds_dwordx4 v[242:243], off
	v_lshl_add_u64 v[242:243], s[6:7], 0, v[174:175]
	s_mov_b32 m0, s42
	s_nop 0
	global_load_lds_dwordx4 v[242:243], off
	s_waitcnt vmcnt(8)
	s_waitcnt lgkmcnt(0)
	s_barrier
	s_setprio 1
	s_waitcnt lgkmcnt(0)
	v_mfma_scale_f32_16x16x128_f8f6f4 v[96:99], v[4:11], v[194:201], v[96:99], v1, v1 op_sel_hi:[0,0,0]
	v_mfma_scale_f32_16x16x128_f8f6f4 v[92:95], v[12:19], v[194:201], v[92:95], v1, v1 op_sel_hi:[0,0,0]
	v_mfma_scale_f32_16x16x128_f8f6f4 v[88:91], v[4:11], v[202:209], v[88:91], v1, v1 op_sel_hi:[0,0,0]
	v_mfma_scale_f32_16x16x128_f8f6f4 v[84:87], v[12:19], v[202:209], v[84:87], v1, v1 op_sel_hi:[0,0,0]
	v_mfma_scale_f32_16x16x128_f8f6f4 v[80:83], v[4:11], v[226:233], v[80:83], v1, v1 op_sel_hi:[0,0,0]
	v_mfma_scale_f32_16x16x128_f8f6f4 v[76:79], v[12:19], v[226:233], v[76:79], v1, v1 op_sel_hi:[0,0,0]
	v_mfma_scale_f32_16x16x128_f8f6f4 v[72:75], v[4:11], v[234:241], v[72:75], v1, v1 op_sel_hi:[0,0,0]
	v_mfma_scale_f32_16x16x128_f8f6f4 v[68:71], v[12:19], v[234:241], v[68:71], v1, v1 op_sel_hi:[0,0,0]
	s_setprio 0
	s_setprio 1
	v_mfma_scale_f32_16x16x128_f8f6f4 v[160:163], v[20:27], v[194:201], v[160:163], v1, v1 op_sel_hi:[0,0,0]
	v_mfma_scale_f32_16x16x128_f8f6f4 v[156:159], v[28:35], v[194:201], v[156:159], v1, v1 op_sel_hi:[0,0,0]
	v_mfma_scale_f32_16x16x128_f8f6f4 v[152:155], v[20:27], v[202:209], v[152:155], v1, v1 op_sel_hi:[0,0,0]
	v_mfma_scale_f32_16x16x128_f8f6f4 v[148:151], v[28:35], v[202:209], v[148:151], v1, v1 op_sel_hi:[0,0,0]
	v_mfma_scale_f32_16x16x128_f8f6f4 v[144:147], v[20:27], v[226:233], v[144:147], v1, v1 op_sel_hi:[0,0,0]
	v_mfma_scale_f32_16x16x128_f8f6f4 v[140:143], v[28:35], v[226:233], v[140:143], v1, v1 op_sel_hi:[0,0,0]
	v_mfma_scale_f32_16x16x128_f8f6f4 v[136:139], v[20:27], v[234:241], v[136:139], v1, v1 op_sel_hi:[0,0,0]
	v_mfma_scale_f32_16x16x128_f8f6f4 v[132:135], v[28:35], v[234:241], v[132:135], v1, v1 op_sel_hi:[0,0,0]
	s_setprio 0
	s_barrier
	s_add_i32 s6, s52, s36
	v_lshl_add_u64 v[184:185], v[184:185], 0, s[56:57]
	s_mov_b32 m0, s6
	ds_read_b128 v[194:197], v193 offset:49152
	ds_read_b128 v[198:201], v250 offset:49152
	ds_read_b128 v[202:205], v193 offset:51200
	ds_read_b128 v[206:209], v250 offset:51200
	ds_read_b128 v[226:229], v193 offset:53248
	ds_read_b128 v[230:233], v250 offset:53248
	ds_read_b128 v[234:237], v193 offset:55296
	ds_read_b128 v[238:241], v250 offset:55296
	global_load_lds_dwordx4 v[184:185], off
	s_add_i32 m0, s6, 0x2000
	s_add_u32 s4, s4, 0x8080
	v_lshl_add_u64 v[184:185], v[186:187], 0, s[56:57]
	s_addc_u32 s5, s5, 0
	s_add_i32 s6, s53, s36
	global_load_lds_dwordx4 v[184:185], off
	v_lshl_add_u64 v[184:185], s[4:5], 0, v[176:177]
	s_mov_b32 m0, s6
	s_nop 0
	global_load_lds_dwordx4 v[184:185], off
	v_lshl_add_u64 v[184:185], s[4:5], 0, v[172:173]
	s_add_i32 m0, s6, 0x2000
	s_nop 0
	global_load_lds_dwordx4 v[184:185], off
	v_lshl_add_u64 v[184:185], v[188:189], 0, s[56:57]
	s_mov_b32 m0, s45
	s_nop 0
	global_load_lds_dwordx4 v[184:185], off
	v_lshl_add_u64 v[184:185], v[190:191], 0, s[56:57]
	s_mov_b32 m0, s46
	s_nop 0
	global_load_lds_dwordx4 v[184:185], off
	s_waitcnt vmcnt(8)
	s_waitcnt lgkmcnt(0)
	s_barrier
	s_setprio 1
	s_waitcnt lgkmcnt(0)
	v_mfma_scale_f32_16x16x128_f8f6f4 v[64:67], v[4:11], v[194:201], v[64:67], v1, v1 op_sel_hi:[0,0,0]
	v_mfma_scale_f32_16x16x128_f8f6f4 v[60:63], v[12:19], v[194:201], v[60:63], v1, v1 op_sel_hi:[0,0,0]
	v_mfma_scale_f32_16x16x128_f8f6f4 v[56:59], v[4:11], v[202:209], v[56:59], v1, v1 op_sel_hi:[0,0,0]
	v_mfma_scale_f32_16x16x128_f8f6f4 v[52:55], v[12:19], v[202:209], v[52:55], v1, v1 op_sel_hi:[0,0,0]
	v_mfma_scale_f32_16x16x128_f8f6f4 v[48:51], v[4:11], v[226:233], v[48:51], v1, v1 op_sel_hi:[0,0,0]
	v_mfma_scale_f32_16x16x128_f8f6f4 v[44:47], v[12:19], v[226:233], v[44:47], v1, v1 op_sel_hi:[0,0,0]
	v_mfma_scale_f32_16x16x128_f8f6f4 v[40:43], v[4:11], v[234:241], v[40:43], v1, v1 op_sel_hi:[0,0,0]
	v_mfma_scale_f32_16x16x128_f8f6f4 v[36:39], v[12:19], v[234:241], v[36:39], v1, v1 op_sel_hi:[0,0,0]
	s_setprio 0
	s_setprio 1
	v_mfma_scale_f32_16x16x128_f8f6f4 v[128:131], v[20:27], v[194:201], v[128:131], v1, v1 op_sel_hi:[0,0,0]
	v_mfma_scale_f32_16x16x128_f8f6f4 v[124:127], v[28:35], v[194:201], v[124:127], v1, v1 op_sel_hi:[0,0,0]
	v_mfma_scale_f32_16x16x128_f8f6f4 v[120:123], v[20:27], v[202:209], v[120:123], v1, v1 op_sel_hi:[0,0,0]
	v_mfma_scale_f32_16x16x128_f8f6f4 v[116:119], v[28:35], v[202:209], v[116:119], v1, v1 op_sel_hi:[0,0,0]
	v_mfma_scale_f32_16x16x128_f8f6f4 v[112:115], v[20:27], v[226:233], v[112:115], v1, v1 op_sel_hi:[0,0,0]
	v_mfma_scale_f32_16x16x128_f8f6f4 v[108:111], v[28:35], v[226:233], v[108:111], v1, v1 op_sel_hi:[0,0,0]
	v_mfma_scale_f32_16x16x128_f8f6f4 v[104:107], v[20:27], v[234:241], v[104:107], v1, v1 op_sel_hi:[0,0,0]
	v_mfma_scale_f32_16x16x128_f8f6f4 v[100:103], v[28:35], v[234:241], v[100:103], v1, v1 op_sel_hi:[0,0,0]
	s_setprio 0
	s_barrier
	s_add_i32 s51, s51, 2
	s_add_u32 s0, s0, 0x100
	s_addc_u32 s1, s1, 0
	s_add_u32 s49, s49, 0x100
	s_addc_u32 s50, s50, 0
	s_cmp_gt_u32 s51, 5
	s_cbranch_scc0 .LBB0_235
	s_and_b64 vcc, exec, s[18:19]
	s_cbranch_vccz .LBB0_238
	s_barrier

.LBB0_245:
	v_and_b32_e32 v11, 0x7fffffff, v14
	v_mov_b64_e32 v[6:7], s[10:11]
	s_movk_i32 s21, 0x2600
	v_mad_u64_u32 v[6:7], s[48:49], v11, s21, v[6:7]
	v_lshlrev_b32_e32 v4, 3, v10
	v_lshl_add_u64 v[12:13], v[6:7], 0, s[6:7]
	v_ashrrev_i32_e32 v5, 31, v4
	v_lshl_add_u64 v[12:13], v[12:13], 0, s[16:17]
	v_lshl_add_u64 v[12:13], v[12:13], 0, v[4:5]
	v_mov_b32_e32 v244, v8
	v_mov_b32_e32 v245, v9
	v_cndmask_b32_e64 v8, 0, 1, s[28:29]
	v_cmp_ne_u32_e64 s[6:7], 1, v8
	s_andn2_b64 vcc, exec, s[28:29]
	s_mov_b64 s[28:29], -1
	s_cbranch_vccnz .LBB0_247
	s_mov_b32 s28, 0x3e800000
	v_pk_mul_f32 v[12:13], v[160:161], s[28:29] op_sel_hi:[1,0]
	v_pk_mul_f32 v[16:17], v[156:157], s[28:29] op_sel_hi:[1,0]
	v_mov_b32_e32 v8, v2
	v_mov_b32_e32 v9, v2
	v_cvt_pk_fp8_f32 v8, v12, v13
	v_cvt_pk_fp8_f32 v9, v16, v17
	v_pk_mul_f32 v[12:13], v[162:163], s[28:29] op_sel_hi:[1,0]
	v_pk_mul_f32 v[16:17], v[158:159], s[28:29] op_sel_hi:[1,0]
	v_cvt_pk_fp8_f32 v8, v12, v13 op_sel:[0,0,1]
	v_cvt_pk_fp8_f32 v9, v16, v17 op_sel:[0,0,1]
	s_mov_b64 s[28:29], 0

.LBB0_251:
	v_lshl_add_u64 v[6:7], v[6:7], 0, s[28:29]
	v_lshl_add_u64 v[6:7], v[6:7], 0, s[16:17]
	v_lshl_add_u64 v[6:7], v[6:7], 0, v[4:5]
	s_and_b64 vcc, exec, s[6:7]
	s_mov_b64 s[28:29], -1
	v_mov_b32_e32 v246, v8
	v_mov_b32_e32 v247, v9
	v_lshl_add_u64 v[6:7], v[6:7], 0, v[4:5]
	s_nop 0
	v_permlane32_swap_b32_e32 v244, v246
	v_permlane32_swap_b32_e32 v245, v247
	s_nop 1
	v_permlane16_swap_b32_e32 v244, v246
	v_permlane16_swap_b32_e32 v245, v247
	s_nop 1
	global_store_dwordx4 v[6:7], v[244:247], off
	s_cbranch_vccnz .LBB0_253
	s_mov_b32 s28, 0x3e800000
	v_pk_mul_f32 v[6:7], v[88:89], s[28:29] op_sel_hi:[1,0]
	v_pk_mul_f32 v[12:13], v[84:85], s[28:29] op_sel_hi:[1,0]
	v_mov_b32_e32 v8, v2
	v_mov_b32_e32 v9, v2
	v_cvt_pk_fp8_f32 v8, v6, v7
	v_cvt_pk_fp8_f32 v9, v12, v13
	v_pk_mul_f32 v[6:7], v[90:91], s[28:29] op_sel_hi:[1,0]
	v_pk_mul_f32 v[12:13], v[86:87], s[28:29] op_sel_hi:[1,0]
	v_cvt_pk_fp8_f32 v8, v6, v7 op_sel:[0,0,1]
	v_cvt_pk_fp8_f32 v9, v12, v13 op_sel:[0,0,1]
	s_mov_b64 s[28:29], 0

.LBB0_257:
	v_add_u32_e32 v6, 16, v14
	v_and_b32_e32 v11, 0x7fffffff, v6
	v_mov_b64_e32 v[6:7], s[10:11]
	v_mad_u64_u32 v[6:7], s[48:49], v11, s21, v[6:7]
	v_lshl_add_u64 v[12:13], v[6:7], 0, s[28:29]
	v_lshl_add_u64 v[12:13], v[12:13], 0, s[16:17]
	v_lshl_add_u64 v[12:13], v[12:13], 0, v[4:5]
	s_and_b64 vcc, exec, s[6:7]
	s_mov_b64 s[28:29], -1
	v_mov_b32_e32 v244, v8
	v_mov_b32_e32 v245, v9
	s_cbranch_vccnz .LBB0_259
	s_mov_b32 s28, 0x3e800000
	v_pk_mul_f32 v[12:13], v[152:153], s[28:29] op_sel_hi:[1,0]
	v_pk_mul_f32 v[16:17], v[148:149], s[28:29] op_sel_hi:[1,0]
	v_mov_b32_e32 v8, v2
	v_mov_b32_e32 v9, v2
	v_cvt_pk_fp8_f32 v8, v12, v13
	v_cvt_pk_fp8_f32 v9, v16, v17
	v_pk_mul_f32 v[12:13], v[154:155], s[28:29] op_sel_hi:[1,0]
	v_pk_mul_f32 v[16:17], v[150:151], s[28:29] op_sel_hi:[1,0]
	v_cvt_pk_fp8_f32 v8, v12, v13 op_sel:[0,0,1]
	v_cvt_pk_fp8_f32 v9, v16, v17 op_sel:[0,0,1]
	s_mov_b64 s[28:29], 0

.LBB0_263:
	v_lshl_add_u64 v[6:7], v[6:7], 0, s[28:29]
	v_lshl_add_u64 v[6:7], v[6:7], 0, s[16:17]
	v_lshl_add_u64 v[6:7], v[6:7], 0, v[4:5]
	s_and_b64 vcc, exec, s[6:7]
	s_mov_b64 s[28:29], -1
	v_mov_b32_e32 v246, v8
	v_mov_b32_e32 v247, v9
	v_lshl_add_u64 v[6:7], v[6:7], 0, v[4:5]
	s_nop 0
	v_permlane32_swap_b32_e32 v244, v246
	v_permlane32_swap_b32_e32 v245, v247
	s_nop 1
	v_permlane16_swap_b32_e32 v244, v246
	v_permlane16_swap_b32_e32 v245, v247
	s_nop 1
	global_store_dwordx4 v[6:7], v[244:247], off
	s_cbranch_vccnz .LBB0_265
	s_mov_b32 s28, 0x3e800000
	v_pk_mul_f32 v[6:7], v[80:81], s[28:29] op_sel_hi:[1,0]
	v_pk_mul_f32 v[12:13], v[76:77], s[28:29] op_sel_hi:[1,0]
	v_mov_b32_e32 v8, v2
	v_mov_b32_e32 v9, v2
	v_cvt_pk_fp8_f32 v8, v6, v7
	v_cvt_pk_fp8_f32 v9, v12, v13
	v_pk_mul_f32 v[6:7], v[82:83], s[28:29] op_sel_hi:[1,0]
	v_pk_mul_f32 v[12:13], v[78:79], s[28:29] op_sel_hi:[1,0]
	v_cvt_pk_fp8_f32 v8, v6, v7 op_sel:[0,0,1]
	v_cvt_pk_fp8_f32 v9, v12, v13 op_sel:[0,0,1]
	s_mov_b64 s[28:29], 0

.LBB0_269:
	v_add_u32_e32 v6, 32, v14
	v_and_b32_e32 v11, 0x7fffffff, v6
	v_mov_b64_e32 v[6:7], s[10:11]
	v_mad_u64_u32 v[6:7], s[48:49], v11, s21, v[6:7]
	v_lshl_add_u64 v[12:13], v[6:7], 0, s[28:29]
	v_lshl_add_u64 v[12:13], v[12:13], 0, s[16:17]
	v_lshl_add_u64 v[12:13], v[12:13], 0, v[4:5]
	s_and_b64 vcc, exec, s[6:7]
	s_mov_b64 s[28:29], -1
	v_mov_b32_e32 v244, v8
	v_mov_b32_e32 v245, v9
	s_cbranch_vccnz .LBB0_271
	s_mov_b32 s28, 0x3e800000
	v_pk_mul_f32 v[12:13], v[144:145], s[28:29] op_sel_hi:[1,0]
	v_pk_mul_f32 v[16:17], v[140:141], s[28:29] op_sel_hi:[1,0]
	v_mov_b32_e32 v8, v2
	v_mov_b32_e32 v9, v2
	v_cvt_pk_fp8_f32 v8, v12, v13
	v_cvt_pk_fp8_f32 v9, v16, v17
	v_pk_mul_f32 v[12:13], v[146:147], s[28:29] op_sel_hi:[1,0]
	v_pk_mul_f32 v[16:17], v[142:143], s[28:29] op_sel_hi:[1,0]
	v_cvt_pk_fp8_f32 v8, v12, v13 op_sel:[0,0,1]
	v_cvt_pk_fp8_f32 v9, v16, v17 op_sel:[0,0,1]
	s_mov_b64 s[28:29], 0

.LBB0_275:
	v_lshl_add_u64 v[6:7], v[6:7], 0, s[28:29]
	v_lshl_add_u64 v[6:7], v[6:7], 0, s[16:17]
	v_lshl_add_u64 v[6:7], v[6:7], 0, v[4:5]
	s_and_b64 vcc, exec, s[6:7]
	s_mov_b64 s[28:29], -1
	v_mov_b32_e32 v246, v8
	v_mov_b32_e32 v247, v9
	v_lshl_add_u64 v[6:7], v[6:7], 0, v[4:5]
	s_nop 0
	v_permlane32_swap_b32_e32 v244, v246
	v_permlane32_swap_b32_e32 v245, v247
	s_nop 1
	v_permlane16_swap_b32_e32 v244, v246
	v_permlane16_swap_b32_e32 v245, v247
	s_nop 1
	global_store_dwordx4 v[6:7], v[244:247], off
	s_cbranch_vccnz .LBB0_277
	s_mov_b32 s28, 0x3e800000
	v_pk_mul_f32 v[6:7], v[72:73], s[28:29] op_sel_hi:[1,0]
	v_pk_mul_f32 v[12:13], v[68:69], s[28:29] op_sel_hi:[1,0]
	v_mov_b32_e32 v8, v2
	v_mov_b32_e32 v9, v2
	v_cvt_pk_fp8_f32 v8, v6, v7
	v_cvt_pk_fp8_f32 v9, v12, v13
	v_pk_mul_f32 v[6:7], v[74:75], s[28:29] op_sel_hi:[1,0]
	v_pk_mul_f32 v[12:13], v[70:71], s[28:29] op_sel_hi:[1,0]
	v_cvt_pk_fp8_f32 v8, v6, v7 op_sel:[0,0,1]
	v_cvt_pk_fp8_f32 v9, v12, v13 op_sel:[0,0,1]
	s_mov_b64 s[28:29], 0

.LBB0_281:
	v_add_u32_e32 v6, 48, v14
	v_and_b32_e32 v11, 0x7fffffff, v6
	v_mov_b64_e32 v[6:7], s[10:11]
	v_mad_u64_u32 v[6:7], s[48:49], v11, s21, v[6:7]
	v_lshl_add_u64 v[12:13], v[6:7], 0, s[28:29]
	v_lshl_add_u64 v[12:13], v[12:13], 0, s[16:17]
	v_lshl_add_u64 v[12:13], v[12:13], 0, v[4:5]
	s_and_b64 vcc, exec, s[6:7]
	s_mov_b64 s[28:29], -1
	v_mov_b32_e32 v244, v8
	v_mov_b32_e32 v245, v9
	s_cbranch_vccnz .LBB0_283
	s_mov_b32 s28, 0x3e800000
	v_pk_mul_f32 v[12:13], v[136:137], s[28:29] op_sel_hi:[1,0]
	v_pk_mul_f32 v[16:17], v[132:133], s[28:29] op_sel_hi:[1,0]
	v_mov_b32_e32 v8, v2
	v_mov_b32_e32 v9, v2
	v_cvt_pk_fp8_f32 v8, v12, v13
	v_cvt_pk_fp8_f32 v9, v16, v17
	v_pk_mul_f32 v[12:13], v[138:139], s[28:29] op_sel_hi:[1,0]
	v_pk_mul_f32 v[16:17], v[134:135], s[28:29] op_sel_hi:[1,0]
	v_cvt_pk_fp8_f32 v8, v12, v13 op_sel:[0,0,1]
	v_cvt_pk_fp8_f32 v9, v16, v17 op_sel:[0,0,1]
	s_mov_b64 s[28:29], 0

.LBB0_287:
	v_lshl_add_u64 v[6:7], v[6:7], 0, s[28:29]
	v_lshl_add_u64 v[6:7], v[6:7], 0, s[16:17]
	v_lshl_add_u64 v[6:7], v[6:7], 0, v[4:5]
	s_and_b64 vcc, exec, s[6:7]
	s_mov_b64 s[28:29], -1
	v_mov_b32_e32 v246, v8
	v_mov_b32_e32 v247, v9
	v_lshl_add_u64 v[6:7], v[6:7], 0, v[4:5]
	s_nop 0
	v_permlane32_swap_b32_e32 v244, v246
	v_permlane32_swap_b32_e32 v245, v247
	s_nop 1
	v_permlane16_swap_b32_e32 v244, v246
	v_permlane16_swap_b32_e32 v245, v247
	s_nop 1
	global_store_dwordx4 v[6:7], v[244:247], off
	s_cbranch_vccnz .LBB0_289
	s_mov_b32 s28, 0x3e800000
	v_pk_mul_f32 v[6:7], v[64:65], s[28:29] op_sel_hi:[1,0]
	v_pk_mul_f32 v[12:13], v[60:61], s[28:29] op_sel_hi:[1,0]
	v_mov_b32_e32 v8, v2
	v_mov_b32_e32 v9, v2
	v_cvt_pk_fp8_f32 v8, v6, v7
	v_cvt_pk_fp8_f32 v9, v12, v13
	v_pk_mul_f32 v[6:7], v[66:67], s[28:29] op_sel_hi:[1,0]
	v_pk_mul_f32 v[12:13], v[62:63], s[28:29] op_sel_hi:[1,0]
	v_cvt_pk_fp8_f32 v8, v6, v7 op_sel:[0,0,1]
	v_cvt_pk_fp8_f32 v9, v12, v13 op_sel:[0,0,1]
	s_mov_b64 s[28:29], 0

.LBB0_293:
	v_add_u32_e32 v6, 0x80, v14
	v_and_b32_e32 v11, 0x7fffffff, v6
	v_mov_b64_e32 v[6:7], s[10:11]
	v_mad_u64_u32 v[6:7], s[48:49], v11, s21, v[6:7]
	v_lshl_add_u64 v[12:13], v[6:7], 0, s[28:29]
	v_lshl_add_u64 v[12:13], v[12:13], 0, s[16:17]
	v_lshl_add_u64 v[12:13], v[12:13], 0, v[4:5]
	s_and_b64 vcc, exec, s[6:7]
	s_mov_b64 s[28:29], -1
	v_mov_b32_e32 v244, v8
	v_mov_b32_e32 v245, v9
	s_cbranch_vccnz .LBB0_295
	s_mov_b32 s28, 0x3e800000
	v_pk_mul_f32 v[12:13], v[128:129], s[28:29] op_sel_hi:[1,0]
	v_pk_mul_f32 v[16:17], v[124:125], s[28:29] op_sel_hi:[1,0]
	v_mov_b32_e32 v8, v2
	v_mov_b32_e32 v9, v2
	v_cvt_pk_fp8_f32 v8, v12, v13
	v_cvt_pk_fp8_f32 v9, v16, v17
	v_pk_mul_f32 v[12:13], v[130:131], s[28:29] op_sel_hi:[1,0]
	v_pk_mul_f32 v[16:17], v[126:127], s[28:29] op_sel_hi:[1,0]
	v_cvt_pk_fp8_f32 v8, v12, v13 op_sel:[0,0,1]
	v_cvt_pk_fp8_f32 v9, v16, v17 op_sel:[0,0,1]
	s_mov_b64 s[28:29], 0

.LBB0_299:
	v_lshl_add_u64 v[6:7], v[6:7], 0, s[28:29]
	v_lshl_add_u64 v[6:7], v[6:7], 0, s[16:17]
	v_lshl_add_u64 v[6:7], v[6:7], 0, v[4:5]
	s_and_b64 vcc, exec, s[6:7]
	s_mov_b64 s[28:29], -1
	v_mov_b32_e32 v246, v8
	v_mov_b32_e32 v247, v9
	v_lshl_add_u64 v[6:7], v[6:7], 0, v[4:5]
	s_nop 0
	v_permlane32_swap_b32_e32 v244, v246
	v_permlane32_swap_b32_e32 v245, v247
	s_nop 1
	v_permlane16_swap_b32_e32 v244, v246
	v_permlane16_swap_b32_e32 v245, v247
	s_nop 1
	global_store_dwordx4 v[6:7], v[244:247], off
	s_cbranch_vccnz .LBB0_301
	s_mov_b32 s28, 0x3e800000
	v_pk_mul_f32 v[6:7], v[56:57], s[28:29] op_sel_hi:[1,0]
	v_pk_mul_f32 v[12:13], v[52:53], s[28:29] op_sel_hi:[1,0]
	v_mov_b32_e32 v8, v2
	v_mov_b32_e32 v9, v2
	v_cvt_pk_fp8_f32 v8, v6, v7
	v_cvt_pk_fp8_f32 v9, v12, v13
	v_pk_mul_f32 v[6:7], v[58:59], s[28:29] op_sel_hi:[1,0]
	v_pk_mul_f32 v[12:13], v[54:55], s[28:29] op_sel_hi:[1,0]
	v_cvt_pk_fp8_f32 v8, v6, v7 op_sel:[0,0,1]
	v_cvt_pk_fp8_f32 v9, v12, v13 op_sel:[0,0,1]
	s_mov_b64 s[28:29], 0

.LBB0_305:
	v_add_u32_e32 v6, 0x90, v14
	v_and_b32_e32 v11, 0x7fffffff, v6
	v_mov_b64_e32 v[6:7], s[10:11]
	v_mad_u64_u32 v[6:7], s[48:49], v11, s21, v[6:7]
	v_lshl_add_u64 v[12:13], v[6:7], 0, s[28:29]
	v_lshl_add_u64 v[12:13], v[12:13], 0, s[16:17]
	v_lshl_add_u64 v[12:13], v[12:13], 0, v[4:5]
	s_and_b64 vcc, exec, s[6:7]
	s_mov_b64 s[28:29], -1
	v_mov_b32_e32 v244, v8
	v_mov_b32_e32 v245, v9
	s_cbranch_vccnz .LBB0_307
	s_mov_b32 s28, 0x3e800000
	v_pk_mul_f32 v[12:13], v[120:121], s[28:29] op_sel_hi:[1,0]
	v_pk_mul_f32 v[16:17], v[116:117], s[28:29] op_sel_hi:[1,0]
	v_mov_b32_e32 v8, v2
	v_mov_b32_e32 v9, v2
	v_cvt_pk_fp8_f32 v8, v12, v13
	v_cvt_pk_fp8_f32 v9, v16, v17
	v_pk_mul_f32 v[12:13], v[122:123], s[28:29] op_sel_hi:[1,0]
	v_pk_mul_f32 v[16:17], v[118:119], s[28:29] op_sel_hi:[1,0]
	v_cvt_pk_fp8_f32 v8, v12, v13 op_sel:[0,0,1]
	v_cvt_pk_fp8_f32 v9, v16, v17 op_sel:[0,0,1]
	s_mov_b64 s[28:29], 0

.LBB0_311:
	v_lshl_add_u64 v[6:7], v[6:7], 0, s[28:29]
	v_lshl_add_u64 v[6:7], v[6:7], 0, s[16:17]
	v_lshl_add_u64 v[6:7], v[6:7], 0, v[4:5]
	s_and_b64 vcc, exec, s[6:7]
	s_mov_b64 s[28:29], -1
	v_mov_b32_e32 v246, v8
	v_mov_b32_e32 v247, v9
	v_lshl_add_u64 v[6:7], v[6:7], 0, v[4:5]
	s_nop 0
	v_permlane32_swap_b32_e32 v244, v246
	v_permlane32_swap_b32_e32 v245, v247
	s_nop 1
	v_permlane16_swap_b32_e32 v244, v246
	v_permlane16_swap_b32_e32 v245, v247
	s_nop 1
	global_store_dwordx4 v[6:7], v[244:247], off
	s_cbranch_vccnz .LBB0_313
	s_mov_b32 s28, 0x3e800000
	v_pk_mul_f32 v[6:7], v[48:49], s[28:29] op_sel_hi:[1,0]
	v_pk_mul_f32 v[12:13], v[44:45], s[28:29] op_sel_hi:[1,0]
	v_mov_b32_e32 v8, v2
	v_mov_b32_e32 v9, v2
	v_cvt_pk_fp8_f32 v8, v6, v7
	v_cvt_pk_fp8_f32 v9, v12, v13
	v_pk_mul_f32 v[6:7], v[50:51], s[28:29] op_sel_hi:[1,0]
	v_pk_mul_f32 v[12:13], v[46:47], s[28:29] op_sel_hi:[1,0]
	v_cvt_pk_fp8_f32 v8, v6, v7 op_sel:[0,0,1]
	v_cvt_pk_fp8_f32 v9, v12, v13 op_sel:[0,0,1]
	s_mov_b64 s[28:29], 0

.LBB0_317:
	v_add_u32_e32 v6, 0xa0, v14
	v_and_b32_e32 v11, 0x7fffffff, v6
	v_mov_b64_e32 v[6:7], s[10:11]
	v_mad_u64_u32 v[6:7], s[48:49], v11, s21, v[6:7]
	v_lshl_add_u64 v[12:13], v[6:7], 0, s[28:29]
	v_lshl_add_u64 v[12:13], v[12:13], 0, s[16:17]
	v_lshl_add_u64 v[12:13], v[12:13], 0, v[4:5]
	s_and_b64 vcc, exec, s[6:7]
	s_mov_b64 s[28:29], -1
	v_mov_b32_e32 v244, v8
	v_mov_b32_e32 v245, v9
	s_cbranch_vccnz .LBB0_319
	s_mov_b32 s28, 0x3e800000
	v_pk_mul_f32 v[12:13], v[112:113], s[28:29] op_sel_hi:[1,0]
	v_pk_mul_f32 v[16:17], v[108:109], s[28:29] op_sel_hi:[1,0]
	v_mov_b32_e32 v8, v2
	v_mov_b32_e32 v9, v2
	v_cvt_pk_fp8_f32 v8, v12, v13
	v_cvt_pk_fp8_f32 v9, v16, v17
	v_pk_mul_f32 v[12:13], v[114:115], s[28:29] op_sel_hi:[1,0]
	v_pk_mul_f32 v[16:17], v[110:111], s[28:29] op_sel_hi:[1,0]
	v_cvt_pk_fp8_f32 v8, v12, v13 op_sel:[0,0,1]
	v_cvt_pk_fp8_f32 v9, v16, v17 op_sel:[0,0,1]
	s_mov_b64 s[28:29], 0

.LBB0_323:
	v_lshl_add_u64 v[6:7], v[6:7], 0, s[28:29]
	v_lshl_add_u64 v[6:7], v[6:7], 0, s[16:17]
	v_lshl_add_u64 v[6:7], v[6:7], 0, v[4:5]
	s_and_b64 vcc, exec, s[6:7]
	s_mov_b64 s[28:29], -1
	v_mov_b32_e32 v246, v8
	v_mov_b32_e32 v247, v9
	v_lshl_add_u64 v[6:7], v[6:7], 0, v[4:5]
	s_nop 0
	v_permlane32_swap_b32_e32 v244, v246
	v_permlane32_swap_b32_e32 v245, v247
	s_nop 1
	v_permlane16_swap_b32_e32 v244, v246
	v_permlane16_swap_b32_e32 v245, v247
	s_nop 1
	global_store_dwordx4 v[6:7], v[244:247], off
	s_cbranch_vccnz .LBB0_325
	s_mov_b32 s28, 0x3e800000
	v_pk_mul_f32 v[6:7], v[40:41], s[28:29] op_sel_hi:[1,0]
	v_pk_mul_f32 v[12:13], v[36:37], s[28:29] op_sel_hi:[1,0]
	v_mov_b32_e32 v8, v2
	v_mov_b32_e32 v9, v2
	v_cvt_pk_fp8_f32 v8, v6, v7
	v_cvt_pk_fp8_f32 v9, v12, v13
	v_pk_mul_f32 v[6:7], v[42:43], s[28:29] op_sel_hi:[1,0]
	v_pk_mul_f32 v[12:13], v[38:39], s[28:29] op_sel_hi:[1,0]
	v_cvt_pk_fp8_f32 v8, v6, v7 op_sel:[0,0,1]
	v_cvt_pk_fp8_f32 v9, v12, v13 op_sel:[0,0,1]
	s_mov_b64 s[28:29], 0

.LBB0_329:
	v_add_u32_e32 v6, 0xb0, v14
	v_and_b32_e32 v11, 0x7fffffff, v6
	v_mov_b64_e32 v[6:7], s[10:11]
	v_mad_u64_u32 v[6:7], s[48:49], v11, s21, v[6:7]
	v_lshl_add_u64 v[12:13], v[6:7], 0, s[28:29]
	v_lshl_add_u64 v[12:13], v[12:13], 0, s[16:17]
	v_lshl_add_u64 v[12:13], v[12:13], 0, v[4:5]
	s_and_b64 vcc, exec, s[6:7]
	s_mov_b64 s[6:7], -1
	v_mov_b32_e32 v244, v8
	v_mov_b32_e32 v245, v9
	s_cbranch_vccnz .LBB0_331
	s_mov_b32 s6, 0x3e800000
	v_pk_mul_f32 v[12:13], v[104:105], s[6:7] op_sel_hi:[1,0]
	v_pk_mul_f32 v[16:17], v[100:101], s[6:7] op_sel_hi:[1,0]
	v_mov_b32_e32 v8, v2
	v_mov_b32_e32 v9, v2
	v_cvt_pk_fp8_f32 v8, v12, v13
	v_cvt_pk_fp8_f32 v9, v16, v17
	v_pk_mul_f32 v[12:13], v[106:107], s[6:7] op_sel_hi:[1,0]
	v_pk_mul_f32 v[16:17], v[102:103], s[6:7] op_sel_hi:[1,0]
	v_cvt_pk_fp8_f32 v8, v12, v13 op_sel:[0,0,1]
	v_cvt_pk_fp8_f32 v9, v16, v17 op_sel:[0,0,1]
	s_mov_b64 s[6:7], 0

.LBB0_335:
	v_lshl_add_u64 v[6:7], v[6:7], 0, s[0:1]
	v_lshl_add_u64 v[6:7], v[6:7], 0, s[16:17]
	v_lshl_add_u64 v[4:5], v[6:7], 0, v[4:5]
	v_mov_b32_e32 v246, v8
	v_mov_b32_e32 v247, v9
	v_lshlrev_b32_e32 v6, 3, v10
	v_mov_b32_e32 v7, v2
	v_lshl_add_u64 v[4:5], v[4:5], 0, v[6:7]
	s_nop 0
	v_permlane32_swap_b32_e32 v244, v246
	v_permlane32_swap_b32_e32 v245, v247
	s_nop 1
	v_permlane16_swap_b32_e32 v244, v246
	v_permlane16_swap_b32_e32 v245, v247
	s_nop 1
	global_store_dwordx4 v[4:5], v[244:247], off
